# rwkv state scan chunk loop: the ten quarter-rate v_mul_lo_u32 in its LDS address arithmetic replaced by full-rate v_mul_u32_u24 (operands are lane indices times small pitches)
# speedup vs baseline: 1.0103x; 1.0023x over previous
; #define LAS __attribute__((address_space(3)))
; __device__ __forceinline__ void rwkv_state_phase(LAS unsigned char* lds, const unsigned char* img, bf16_t* y_, const RwScan& a_, const int vcu, const int G, const int tid0_) {
;     ...
;             if (wave < 4) {
;                 { const int o_ = (tid >> 3) * 144 + (tid & 7) * 16; *(LAS u32x4*)(lb + SK_AT + o_) = q0a; *(LAS u32x4*)(lb + SK_RT + o_) = q0b; }
;                 { const int idx = tid & 127, o_ = (tid >> 7) * 2560 + (idx >> 2) * 80 + (idx & 3) * 16; *(LAS u32x4*)(lb + SK_NAK + o_) = q1a; *(LAS u32x4*)(lb + SK_MKR + o_) = q1b; }
;                 { const int o_ = (tid >> 2) * 80 + (tid & 3) * 16; *(LAS u32x4*)(lb + SK_BH + o_) = q2a; *(LAS u32x4*)(lb + SK_KH + o_) = q2b; }
;                 if (tid < 128) { const int t_ = tid >> 2, i0_ = 8 * (tid & 3); const unsigned wv_[4] = {q3.x, q3.y, q3.z, q3.w};
; #pragma unroll
;                     for (int e = 0; e < 4; ++e) { Vi[(i0_ + 2 * e) * P32 + t_] = (bf16_t)(wv_[e] & 0xffffu); Vi[(i0_ + 2 * e + 1) * P32 + t_] = (bf16_t)(wv_[e] >> 16); } }
;                 else if (tid < 144) *(LAS u32x4*)(lb + SK_PL + (tid - 128) * 16) = q3;
.LBB0_747:
	s_bitcmp1_b32 s64, 0
	s_cselect_b32 s10, 0xa500, 0
	v_mov_b32_e32 v2, v1
	s_and_b64 vcc, exec, s[8:9]
	s_add_i32 s65, s10, 0
	s_cbranch_vccnz .LBB0_755
	v_lshrrev_b32_e32 v4, 3, v2
	v_mul_u32_u24_e32 v5, s67, v4
	v_lshlrev_b32_e32 v4, 4, v2
	v_and_b32_e32 v79, 0x70, v4
	v_add3_u32 v5, v5, v79, s65
	s_waitcnt vmcnt(5)
	ds_write_b128 v5, v[42:45]
	s_waitcnt vmcnt(4)
	ds_write_b128 v5, v[46:49] offset:4608
	v_lshrrev_b32_e32 v5, 7, v2
	s_movk_i32 s10, 0xa00
	v_mul_u32_u24_e32 v5, s10, v5
	v_bfe_u32 v79, v2, 2, 5
	v_mul_u32_u24_e32 v79, 0x50, v79
	v_and_or_b32 v5, v4, 48, v5
	v_add3_u32 v5, v5, v79, s65
	s_waitcnt vmcnt(3)
	ds_write_b128 v5, v[50:53] offset:13824
	s_waitcnt vmcnt(2)
	ds_write_b128 v5, v[54:57] offset:18944
	v_ashrrev_i32_e32 v5, 2, v2
	v_and_b32_e32 v79, 3, v2
	v_mul_u32_u24_e32 v81, s66, v5
	v_lshlrev_b32_e32 v94, 4, v79
	s_movk_i32 s10, 0x7f
	v_add3_u32 v81, v81, v94, s65
	v_cmp_lt_i32_e32 vcc, s10, v2
	s_waitcnt vmcnt(1)
	ds_write_b128 v81, v[58:61] offset:31744
	s_waitcnt vmcnt(0)
	ds_write_b128 v81, v[66:69] offset:36864
	s_and_saveexec_b64 s[10:11], vcc
	s_xor_b64 s[10:11], exec, s[10:11]
	s_cbranch_execz .LBB0_752
	v_cmp_gt_u32_e32 vcc, s67, v2
	s_and_saveexec_b64 s[34:35], vcc
	v_add_u32_e32 v4, s65, v4
	ds_write_b128 v4, v[38:41] offset:39936
	s_or_b64 exec, exec, s[34:35]

; #define LAS __attribute__((address_space(3)))
; __device__ __forceinline__ unsigned cvt_pk_bf16(float lo, float hi) { const f32x2 v = {lo, hi}; const bf16x2_t b = __builtin_convertvector(v, bf16x2_t); return __builtin_bit_cast(unsigned, b); }
; #define ZERO4() ((f32x4){opaque0(), 0.f, 0.f, 0.f} * 0.f)
; __device__ __forceinline__ void rwkv_state_phase(LAS unsigned char* lds, const unsigned char* img, bf16_t* y_, const RwScan& a_, const int vcu, const int G, const int tid0_) {
;     ...
;             if (wave >= 4) {
;                 const int mt = (wave - 4) >> 1, nt = (wave - 4) & 1;
;                 f32x4 w = ZERO4();
; #pragma unroll
;                 for (int ks = 0; ks < 2; ++ks) w = __builtin_amdgcn_mfma_f32_16x16x32_bf16(ldfrag(AT, P64, 16 * mt + fr, 32 * ks + 8 * fq), ldfrag(S0, P64, 16 * nt + fr, 32 * ks + 8 * fq), w, 0, 0, 0);
;                 w = __builtin_amdgcn_mfma_f32_16x16x32_bf16(ldfrag(NakT, P32, 16 * mt + fr, 8 * fq), ldfrag(Vi, P32, 16 * nt + fr, 8 * fq), w, 0, 0, 0);
;                 u32x2 o; o.x = cvt_pk_bf16(w[0], w[1]); o.y = cvt_pk_bf16(w[2], w[3]); *(LAS u32x2*)(Wi + (16 * nt + fr) * P32 + 16 * mt + 4 * fq) = o;
;             }
;             __syncthreads();
;             if (wave < 4) {
;                 const int mt = wave >> 1, nt = wave & 1;
;                 f32x4 uu = ZERO4();
;                 uu = __builtin_amdgcn_mfma_f32_16x16x32_bf16(ldfrag(TT, P32, 16 * mt + fr, 8 * fq), ldfrag(Wi, P32, 16 * nt + fr, 8 * fq), uu, 0, 0, 0);
;                 u32x2 o; o.x = cvt_pk_bf16(uu[0], uu[1]); o.y = cvt_pk_bf16(uu[2], uu[3]); *(LAS u32x2*)(Ui + (16 * nt + fr) * P32 + 16 * mt + 4 * fq) = o;
;             }
.LBB0_763:
	v_lshlrev_b32_e32 v97, 2, v96
	v_cndmask_b32_e64 v4, 0, 1, s[16:17]
	v_lshlrev_b32_e32 v99, 4, v96
	v_cmp_ne_u32_e64 s[10:11], 1, v4
	s_andn2_b64 vcc, exec, s[16:17]
	v_mul_u32_u24_e32 v101, 0x50, v95
	v_lshlrev_b32_e32 v94, 1, v97
	v_add_u32_e32 v98, v2, v99
	s_cbranch_vccnz .LBB0_765
	v_or_b32_e32 v100, s55, v81
	v_mul_u32_u24_e32 v102, s67, v100
	v_mov_b32_e32 v2, v3
	v_add3_u32 v110, s65, v102, v99
	v_mul_u32_u24_e32 v114, s66, v100
	v_add3_u32 v115, s65, v101, v99
	v_add3_u32 v114, s65, v114, v99
	ds_read_b128 v[102:105], v110
	ds_read_b128 v[106:109], v98 offset:9216
	ds_read_b128 v[160:163], v110 offset:64
	ds_read_b128 v[164:167], v98 offset:9280
	ds_read_b128 v[168:171], v114 offset:13824
	ds_read_b128 v[172:175], v115 offset:24064
	v_mul_f32_e32 v2, 0, v2
	v_mov_b32_e32 v4, v3
	v_mov_b32_e32 v5, v3
	s_waitcnt lgkmcnt(4)
	s_nop 0
	v_mfma_f32_16x16x32_bf16 v[102:105], v[102:105], v[106:109], v[2:5]
	s_waitcnt lgkmcnt(2)
	v_mfma_f32_16x16x32_bf16 v[102:105], v[160:163], v[164:167], v[102:105]
	s_waitcnt lgkmcnt(0)
	v_mfma_f32_16x16x32_bf16 v[102:105], v[168:171], v[172:175], v[102:105]
	v_add3_u32 v2, s56, v101, v94
	s_nop 7
	v_cvt_pk_bf16_f32 v4, v102, v103
	v_cvt_pk_bf16_f32 v5, v104, v105
	ds_write_b64 v2, v[4:5] offset:26560
.LBB0_765:
	s_and_b64 vcc, exec, s[8:9]
	v_or_b32_e32 v100, s18, v81
	s_waitcnt lgkmcnt(0)
	s_barrier
	s_cbranch_vccnz .LBB0_767
	v_mul_u32_u24_e32 v4, s66, v100
	v_mov_b32_e32 v2, v3
	v_add3_u32 v4, s65, v4, v99
	ds_read_b128 v[102:105], v4 offset:21504
	v_add3_u32 v4, 0, v101, v99
	ds_read_b128 v[106:109], v4 offset:26624
	v_mov_b32_e32 v4, v3
	v_mov_b32_e32 v5, v3
	v_mul_f32_e32 v2, 0, v2
	s_waitcnt lgkmcnt(0)
	s_nop 0
	v_mfma_f32_16x16x32_bf16 v[102:105], v[102:105], v[106:109], v[2:5]
	s_nop 2
	v_add3_u32 v2, s57, v101, v94
	s_nop 3
	v_cvt_pk_bf16_f32 v4, v102, v103
	v_cvt_pk_bf16_f32 v5, v104, v105
	ds_write_b64 v2, v[4:5] offset:29184

; __device__ __forceinline__ unsigned cvt_pk_bf16(float lo, float hi) { const f32x2 v = {lo, hi}; const bf16x2_t b = __builtin_convertvector(v, bf16x2_t); return __builtin_bit_cast(unsigned, b); }
; #define ZERO4() ((f32x4){opaque0(), 0.f, 0.f, 0.f} * 0.f)
; __device__ __forceinline__ void rwkv_state_phase(LAS unsigned char* lds, const unsigned char* img, bf16_t* y_, const RwScan& a_, const int vcu, const int G, const int tid0_) {
;     ...
;             if (wave < 4) {
;                 const int mt = wave >> 1, nt = wave & 1;
;                 f32x4 y = ZERO4();
; #pragma unroll
;                 for (int ks = 0; ks < 2; ++ks) y = __builtin_amdgcn_mfma_f32_16x16x32_bf16(ldfrag(S0, P64, 16 * mt + fr, 32 * ks + 8 * fq), ldfrag(RT, P64, 16 * nt + fr, 32 * ks + 8 * fq), y, 0, 0, 0);
;                 y = __builtin_amdgcn_mfma_f32_16x16x32_bf16(ldfrag(Ui, P32, 16 * mt + fr, 8 * fq), ldfrag(MbrT, P32, 16 * nt + fr, 8 * fq), y, 0, 0, 0);
;                 y = __builtin_amdgcn_mfma_f32_16x16x32_bf16(ldfrag(Vi, P32, 16 * mt + fr, 8 * fq), ldfrag(MkrT, P32, 16 * nt + fr, 8 * fq), y, 0, 0, 0);
;                 u32x2 o; o.x = cvt_pk_bf16(y[0], y[1]); o.y = cvt_pk_bf16(y[2], y[3]);
;                 *(u32x2*)(y_ + (size_t)(b * SEQ + t0 + 16 * nt + fr) * 1024 + h * 64 + half * 32 + 16 * mt + 4 * fq) = o;
;             }
.LBB0_802:
	s_mov_b64 s[34:35], -1
	s_andn2_b64 vcc, exec, s[10:11]
	v_mul_u32_u24_e32 v101, 40, v95
	s_waitcnt lgkmcnt(0)
	s_barrier
	s_cbranch_vccnz .LBB0_804
	v_lshlrev_b32_e32 v5, 3, v96
	v_mul_u32_u24_e32 v2, 40, v100
	v_mul_u32_u24_e32 v4, 40, v95
	s_mov_b64 s[34:35], 0
.LBB0_804:
	s_andn2_b64 vcc, exec, s[34:35]
	s_cbranch_vccnz .LBB0_746
	v_or_b32_e32 v118, s55, v81
	v_mul_u32_u24_e32 v96, s67, v118
	v_mov_b32_e32 v2, v3
	v_add3_u32 v96, s65, v96, v99
	v_mul_u32_u24_e32 v114, 40, v118
	v_lshlrev_b32_e32 v116, 6, v95
	v_lshlrev_b32_e32 v117, 6, v118
	v_lshlrev_b32_e32 v115, 1, v114
	v_sub_u32_e32 v116, v98, v116
	v_sub_u32_e32 v117, v96, v117
	v_add3_u32 v115, 0, v115, v99
	ds_read_b128 v[102:105], v96 offset:9216
	ds_read_b128 v[106:109], v98 offset:4608
	ds_read_b128 v[160:163], v96 offset:9280
	ds_read_b128 v[164:167], v98 offset:4672
	ds_read_b128 v[168:171], v115 offset:29184
	ds_read_b128 v[172:175], v116 offset:16384
	ds_read_b128 v[176:179], v117 offset:24064
	ds_read_b128 v[180:183], v116 offset:18944
	v_mul_f32_e32 v2, 0, v2
	v_mov_b32_e32 v4, v3
	v_mov_b32_e32 v5, v3
	s_waitcnt lgkmcnt(6)
	s_nop 0
	v_mfma_f32_16x16x32_bf16 v[102:105], v[102:105], v[106:109], v[2:5]
	v_add_u32_e32 v98, s33, v81
	v_ashrrev_i32_e32 v99, 31, v98
	s_waitcnt lgkmcnt(4)
	v_mfma_f32_16x16x32_bf16 v[102:105], v[160:163], v[164:167], v[102:105]
	s_waitcnt lgkmcnt(2)
	v_mfma_f32_16x16x32_bf16 v[102:105], v[168:171], v[172:175], v[102:105]
	v_mul_u32_u24_e32 v2, 40, v100
	s_waitcnt lgkmcnt(0)
	v_mfma_f32_16x16x32_bf16 v[102:105], v[176:179], v[180:183], v[102:105]
	v_lshlrev_b64 v[98:99], 11, v[98:99]
	v_lshl_add_u64 v[98:99], s[2:3], 0, v[98:99]
	v_mov_b32_e32 v95, v3
	s_nop 4
	v_cvt_pk_bf16_f32 v4, v102, v103
	v_cvt_pk_bf16_f32 v5, v104, v105
	v_lshl_add_u64 v[94:95], v[98:99], 0, v[94:95]
	global_store_dwordx2 v[94:95], v[4:5], off offset:-64
	v_mov_b32_e32 v4, v101
	v_mov_b32_e32 v5, v79
	s_branch .LBB0_746
